# helper_fc: fc_W fragments converted before the h polls, first-half MFMAs before second poll, older direction polled first for t>=15 (shorter LSTM launch tail)
# speedup vs baseline: 1.0315x; 1.0035x over previous
.LBB0_91:
	s_cmp_lt_i32 s4, 30
	s_movk_i32 s2, 0x80
	s_cselect_b64 s[0:1], -1, 0
	v_cmp_gt_u32_e32 vcc, s2, v0
	s_and_b64 s[0:1], s[0:1], vcc
	s_and_saveexec_b64 s[2:3], s[0:1]
	s_cbranch_execz .LBB0_100
	v_and_b32_e32 v46, 15, v0
	v_and_or_b32 v197, v1, 16, v46
	v_bfe_u32 v196, v0, 4, 2
	v_lshlrev_b32_e32 v0, 9, v197
	v_cmp_gt_u32_e64 s[0:1], 30, v197
	v_mov_b32_e32 v45, 0
	v_mov_b32_e32 v198, 0
	v_cndmask_b32_e64 v0, 0, v0, s[0:1]
	v_lshlrev_b32_e32 v44, 2, v0
	v_lshl_add_u64 v[0:1], s[20:21], 0, v[44:45]
	v_lshlrev_b32_e32 v44, 5, v196
	v_lshl_add_u64 v[4:5], v[0:1], 0, v[44:45]
	s_cmp_gt_i32 s4, 14
	s_cselect_b32 s6, 0x400, 0
	s_mov_b32 s7, 0
	v_lshl_add_u64 v[192:193], v[4:5], 0, s[6:7]
	s_sub_u32 s6, 0, s6
	s_subb_u32 s7, 0, 0
	v_lshl_add_u64 v[4:5], v[4:5], 0, s[6:7]
	global_load_dwordx4 v[188:191], v[192:193], off offset:16
	global_load_dwordx4 v[148:151], v[192:193], off
	global_load_dwordx4 v[184:187], v[192:193], off offset:144
	global_load_dwordx4 v[160:163], v[192:193], off offset:128
	global_load_dwordx4 v[176:179], v[192:193], off offset:272
	global_load_dwordx4 v[180:183], v[192:193], off offset:256
	global_load_dwordx4 v[168:171], v[192:193], off offset:400
	global_load_dwordx4 v[172:175], v[192:193], off offset:384
	global_load_dwordx4 v[156:159], v[192:193], off offset:528
	global_load_dwordx4 v[164:167], v[192:193], off offset:512
	global_load_dwordx4 v[136:139], v[192:193], off offset:656
	global_load_dwordx4 v[144:147], v[192:193], off offset:640
	global_load_dwordx4 v[140:143], v[192:193], off offset:784
	global_load_dwordx4 v[152:155], v[192:193], off offset:768
	global_load_dwordx4 v[128:131], v[192:193], off offset:912
	global_load_dwordx4 v[132:135], v[192:193], off offset:896
	global_load_dwordx4 v[120:123], v[4:5], off offset:1040
	global_load_dwordx4 v[124:127], v[4:5], off offset:1024
	global_load_dwordx4 v[112:115], v[4:5], off offset:1168
	global_load_dwordx4 v[116:119], v[4:5], off offset:1152
	global_load_dwordx4 v[40:43], v[4:5], off offset:1296
	global_load_dwordx4 v[108:111], v[4:5], off offset:1280
	global_load_dwordx4 v[32:35], v[4:5], off offset:1424
	global_load_dwordx4 v[36:39], v[4:5], off offset:1408
	global_load_dwordx4 v[24:27], v[4:5], off offset:1552
	global_load_dwordx4 v[28:31], v[4:5], off offset:1536
	global_load_dwordx4 v[16:19], v[4:5], off offset:1680
	global_load_dwordx4 v[20:23], v[4:5], off offset:1664
	global_load_dwordx4 v[8:11], v[4:5], off offset:1808
	global_load_dwordx4 v[12:15], v[4:5], off offset:1792
	global_load_dwordx4 v[0:3], v[4:5], off offset:1936
	s_nop 0
	global_load_dwordx4 v[4:7], v[4:5], off offset:1920
	s_and_saveexec_b64 s[2:3], s[0:1]
	s_cbranch_execz .LBB0_94
	v_lshlrev_b32_e32 v44, 2, v197
	global_load_dword v198, v44, s[22:23]
.LBB0_94:
	s_or_b64 exec, exec, s[2:3]
	v_lshlrev_b32_e32 v44, 8, v196
	v_lshl_add_u64 v[48:49], s[10:11], 0, v[44:45]
	v_lshlrev_b32_e32 v44, 4, v46
	s_ashr_i32 s5, s4, 31
	v_lshl_add_u64 v[56:57], v[48:49], 0, v[44:45]
	s_lshl_b64 s[2:3], s[4:5], 13
	v_lshl_add_u64 v[44:45], v[56:57], 0, s[2:3]
	s_mov_b32 s6, 0xb4000
	s_cmp_gt_i32 s4, 14
	s_cselect_b32 s2, s6, 0x78000
	s_mov_b32 s3, 0
	v_lshl_add_u64 v[58:59], v[44:45], 0, s[2:3]
	s_mov_b32 s6, 0xb5000
	s_cmp_gt_i32 s4, 14
	s_cselect_b32 s2, s6, 0x79000
	s_mov_b32 s3, 0
	v_lshl_add_u64 v[64:65], v[44:45], 0, s[2:3]
	s_waitcnt vmcnt(0)
	s_mov_b32 s2, 0x43800000
	v_pk_mul_f32 v[148:149], v[148:149], s[2:3] op_sel_hi:[1,0]
	v_pk_mul_f32 v[150:151], v[150:151], s[2:3] op_sel_hi:[1,0]
	v_cvt_pk_f16_f32 v148, v148, v149
	v_cvt_pk_f16_f32 v149, v150, v151
	v_pk_mul_f32 v[150:151], v[188:189], s[2:3] op_sel_hi:[1,0]
	v_pk_mul_f32 v[188:189], v[190:191], s[2:3] op_sel_hi:[1,0]
	v_cvt_pk_f16_f32 v150, v150, v151
	v_cvt_pk_f16_f32 v151, v188, v189
	v_pk_mul_f32 v[160:161], v[160:161], s[2:3] op_sel_hi:[1,0]
	v_pk_mul_f32 v[162:163], v[162:163], s[2:3] op_sel_hi:[1,0]
	v_cvt_pk_f16_f32 v160, v160, v161
	v_cvt_pk_f16_f32 v161, v162, v163
	v_pk_mul_f32 v[162:163], v[184:185], s[2:3] op_sel_hi:[1,0]
	v_pk_mul_f32 v[184:185], v[186:187], s[2:3] op_sel_hi:[1,0]
	v_cvt_pk_f16_f32 v162, v162, v163
	v_cvt_pk_f16_f32 v163, v184, v185
	v_pk_mul_f32 v[180:181], v[180:181], s[2:3] op_sel_hi:[1,0]
	v_pk_mul_f32 v[182:183], v[182:183], s[2:3] op_sel_hi:[1,0]
	v_mul_f32_e64 v176, v176, s2
	v_mul_f32_e64 v177, v177, s2
	v_cvt_pk_f16_f32 v180, v180, v181
	v_cvt_pk_f16_f32 v181, v182, v183
	v_cvt_pk_f16_f32 v182, v176, v177
	v_pk_mul_f32 v[176:177], v[178:179], s[2:3] op_sel_hi:[1,0]
	v_pk_mul_f32 v[172:173], v[172:173], s[2:3] op_sel_hi:[1,0]
	v_cvt_pk_f16_f32 v183, v176, v177
	v_pk_mul_f32 v[174:175], v[174:175], s[2:3] op_sel_hi:[1,0]
	v_pk_mul_f32 v[168:169], v[168:169], s[2:3] op_sel_hi:[1,0]
	v_cvt_pk_f16_f32 v172, v172, v173
	v_cvt_pk_f16_f32 v173, v174, v175
	v_cvt_pk_f16_f32 v174, v168, v169
	v_pk_mul_f32 v[168:169], v[170:171], s[2:3] op_sel_hi:[1,0]
	v_pk_mul_f32 v[164:165], v[164:165], s[2:3] op_sel_hi:[1,0]
	v_cvt_pk_f16_f32 v175, v168, v169
	v_pk_mul_f32 v[166:167], v[166:167], s[2:3] op_sel_hi:[1,0]
	v_pk_mul_f32 v[156:157], v[156:157], s[2:3] op_sel_hi:[1,0]
	v_cvt_pk_f16_f32 v164, v164, v165
	v_cvt_pk_f16_f32 v165, v166, v167
	v_cvt_pk_f16_f32 v166, v156, v157
	v_pk_mul_f32 v[156:157], v[158:159], s[2:3] op_sel_hi:[1,0]
	v_pk_mul_f32 v[144:145], v[144:145], s[2:3] op_sel_hi:[1,0]
	v_cvt_pk_f16_f32 v167, v156, v157
	v_pk_mul_f32 v[146:147], v[146:147], s[2:3] op_sel_hi:[1,0]
	v_pk_mul_f32 v[136:137], v[136:137], s[2:3] op_sel_hi:[1,0]
	v_cvt_pk_f16_f32 v144, v144, v145
	v_cvt_pk_f16_f32 v145, v146, v147
	v_cvt_pk_f16_f32 v146, v136, v137
	v_pk_mul_f32 v[136:137], v[138:139], s[2:3] op_sel_hi:[1,0]
	v_pk_mul_f32 v[138:139], v[154:155], s[2:3] op_sel_hi:[1,0]
	v_cvt_pk_f16_f32 v147, v136, v137
	v_pk_mul_f32 v[136:137], v[152:153], s[2:3] op_sel_hi:[1,0]
	v_pk_mul_f32 v[132:133], v[132:133], s[2:3] op_sel_hi:[1,0]
	v_cvt_pk_f16_f32 v136, v136, v137
	v_cvt_pk_f16_f32 v137, v138, v139
	v_pk_mul_f32 v[138:139], v[140:141], s[2:3] op_sel_hi:[1,0]
	v_pk_mul_f32 v[140:141], v[142:143], s[2:3] op_sel_hi:[1,0]
	v_cvt_pk_f16_f32 v138, v138, v139
	v_cvt_pk_f16_f32 v139, v140, v141
	v_pk_mul_f32 v[134:135], v[134:135], s[2:3] op_sel_hi:[1,0]
	v_pk_mul_f32 v[128:129], v[128:129], s[2:3] op_sel_hi:[1,0]
	v_cvt_pk_f16_f32 v132, v132, v133
	v_cvt_pk_f16_f32 v133, v134, v135
	v_cvt_pk_f16_f32 v134, v128, v129
	v_pk_mul_f32 v[128:129], v[130:131], s[2:3] op_sel_hi:[1,0]
	v_pk_mul_f32 v[124:125], v[124:125], s[2:3] op_sel_hi:[1,0]
	v_cvt_pk_f16_f32 v135, v128, v129
	v_pk_mul_f32 v[126:127], v[126:127], s[2:3] op_sel_hi:[1,0]
	v_pk_mul_f32 v[120:121], v[120:121], s[2:3] op_sel_hi:[1,0]
	v_cvt_pk_f16_f32 v124, v124, v125
	v_cvt_pk_f16_f32 v125, v126, v127
	v_cvt_pk_f16_f32 v126, v120, v121
	v_pk_mul_f32 v[120:121], v[122:123], s[2:3] op_sel_hi:[1,0]
	v_pk_mul_f32 v[116:117], v[116:117], s[2:3] op_sel_hi:[1,0]
	v_cvt_pk_f16_f32 v127, v120, v121
	v_pk_mul_f32 v[118:119], v[118:119], s[2:3] op_sel_hi:[1,0]
	v_pk_mul_f32 v[112:113], v[112:113], s[2:3] op_sel_hi:[1,0]
	v_cvt_pk_f16_f32 v116, v116, v117
	v_cvt_pk_f16_f32 v117, v118, v119
	v_cvt_pk_f16_f32 v118, v112, v113
	v_pk_mul_f32 v[112:113], v[114:115], s[2:3] op_sel_hi:[1,0]
	v_pk_mul_f32 v[108:109], v[108:109], s[2:3] op_sel_hi:[1,0]
	v_cvt_pk_f16_f32 v119, v112, v113
	v_pk_mul_f32 v[110:111], v[110:111], s[2:3] op_sel_hi:[1,0]
	v_pk_mul_f32 v[40:41], v[40:41], s[2:3] op_sel_hi:[1,0]
	v_cvt_pk_f16_f32 v108, v108, v109
	v_cvt_pk_f16_f32 v109, v110, v111
	v_cvt_pk_f16_f32 v110, v40, v41
	v_pk_mul_f32 v[40:41], v[42:43], s[2:3] op_sel_hi:[1,0]
	v_pk_mul_f32 v[36:37], v[36:37], s[2:3] op_sel_hi:[1,0]
	v_cvt_pk_f16_f32 v111, v40, v41
	v_pk_mul_f32 v[38:39], v[38:39], s[2:3] op_sel_hi:[1,0]
	v_pk_mul_f32 v[32:33], v[32:33], s[2:3] op_sel_hi:[1,0]
	v_cvt_pk_f16_f32 v36, v36, v37
	v_cvt_pk_f16_f32 v37, v38, v39
	v_cvt_pk_f16_f32 v38, v32, v33
	v_pk_mul_f32 v[32:33], v[34:35], s[2:3] op_sel_hi:[1,0]
	v_pk_mul_f32 v[28:29], v[28:29], s[2:3] op_sel_hi:[1,0]
	v_cvt_pk_f16_f32 v39, v32, v33
	v_pk_mul_f32 v[30:31], v[30:31], s[2:3] op_sel_hi:[1,0]
	v_pk_mul_f32 v[24:25], v[24:25], s[2:3] op_sel_hi:[1,0]
	v_cvt_pk_f16_f32 v28, v28, v29
	v_cvt_pk_f16_f32 v29, v30, v31
	v_cvt_pk_f16_f32 v30, v24, v25
	v_pk_mul_f32 v[24:25], v[26:27], s[2:3] op_sel_hi:[1,0]
	v_pk_mul_f32 v[20:21], v[20:21], s[2:3] op_sel_hi:[1,0]
	v_cvt_pk_f16_f32 v31, v24, v25
	v_pk_mul_f32 v[22:23], v[22:23], s[2:3] op_sel_hi:[1,0]
	v_pk_mul_f32 v[16:17], v[16:17], s[2:3] op_sel_hi:[1,0]
	v_cvt_pk_f16_f32 v20, v20, v21
	v_cvt_pk_f16_f32 v21, v22, v23
	v_cvt_pk_f16_f32 v22, v16, v17
	v_pk_mul_f32 v[16:17], v[18:19], s[2:3] op_sel_hi:[1,0]
	v_pk_mul_f32 v[12:13], v[12:13], s[2:3] op_sel_hi:[1,0]
	v_cvt_pk_f16_f32 v23, v16, v17
	v_pk_mul_f32 v[14:15], v[14:15], s[2:3] op_sel_hi:[1,0]
	v_pk_mul_f32 v[8:9], v[8:9], s[2:3] op_sel_hi:[1,0]
	v_cvt_pk_f16_f32 v12, v12, v13
	v_cvt_pk_f16_f32 v13, v14, v15
	v_cvt_pk_f16_f32 v14, v8, v9
	v_pk_mul_f32 v[8:9], v[10:11], s[2:3] op_sel_hi:[1,0]
	v_pk_mul_f32 v[4:5], v[4:5], s[2:3] op_sel_hi:[1,0]
	v_cvt_pk_f16_f32 v15, v8, v9
	v_pk_mul_f32 v[6:7], v[6:7], s[2:3] op_sel_hi:[1,0]
	v_pk_mul_f32 v[0:1], v[0:1], s[2:3] op_sel_hi:[1,0]
	v_cvt_pk_f16_f32 v4, v4, v5
	v_cvt_pk_f16_f32 v5, v6, v7
	v_cvt_pk_f16_f32 v6, v0, v1
	v_pk_mul_f32 v[0:1], v[2:3], s[2:3] op_sel_hi:[1,0]
	v_cvt_pk_f16_f32 v7, v0, v1
	v_mov_b32_e32 v66, 0xfffff
	s_mov_b32 s2, 0xfffeffff
.LBB0_95:
	global_load_dwordx4 v[92:95], v[58:59], off sc1
	global_load_dwordx4 v[84:87], v[58:59], off offset:1024 sc1
	global_load_dwordx4 v[76:79], v[58:59], off offset:2048 sc1
	global_load_dwordx4 v[68:71], v[58:59], off offset:3072 sc1
	global_load_dwordx4 v[60:63], v[64:65], off sc1
	global_load_dwordx4 v[52:55], v[64:65], off offset:1024 sc1
	global_load_dwordx4 v[48:51], v[64:65], off offset:2048 sc1
	global_load_dwordx4 v[44:47], v[64:65], off offset:3072 sc1
	s_waitcnt vmcnt(0)
	s_nop 0
	v_max_u32_e32 v67, v85, v87
	v_max_u32_e32 v72, v77, v79
	v_max_u32_e32 v73, v69, v71
	v_max3_u32 v67, v93, v95, v67
	v_max_u32_e32 v74, v61, v63
	v_max3_u32 v67, v67, v72, v73
	v_max_u32_e32 v72, v53, v55
	v_max3_u32 v67, v67, v74, v72
	v_max_u32_e32 v72, v49, v51
	v_max_u32_e32 v73, v45, v47
	v_max3_u32 v67, v67, v72, v73
	v_cmp_lt_u32_e32 vcc, s2, v67
	s_cmp_eq_u64 vcc, 0
	s_cselect_b64 s[6:7], -1, 0
	v_subrev_co_u32_e32 v66, vcc, 1, v66
	s_or_b64 s[6:7], s[6:7], vcc
	s_andn2_b64 vcc, exec, s[6:7]
	s_cbranch_vccnz .LBB0_95
	v_mfma_f32_16x16x32_f16 a[0:3], v[92:95], v[148:151], 0
	v_mfma_f32_16x16x32_f16 a[0:3], v[84:87], v[160:163], a[0:3]
	v_mfma_f32_16x16x32_f16 a[0:3], v[76:79], v[180:183], a[0:3]
	v_mfma_f32_16x16x32_f16 a[0:3], v[68:71], v[172:175], a[0:3]
	v_mfma_f32_16x16x32_f16 a[0:3], v[60:63], v[164:167], a[0:3]
	v_mfma_f32_16x16x32_f16 a[0:3], v[52:55], v[144:147], a[0:3]
	v_mfma_f32_16x16x32_f16 a[0:3], v[48:51], v[136:139], a[0:3]
	v_mfma_f32_16x16x32_f16 a[0:3], v[44:47], v[132:135], a[0:3]
	s_lshl_b64 s[2:3], s[4:5], 13
	v_lshl_add_u64 v[56:57], v[56:57], 0, s[2:3]
	s_mov_b32 s6, 0x78000
	s_cmp_gt_i32 s4, 14
	s_cselect_b32 s2, s6, 0xb4000
	s_mov_b32 s3, 0
	v_lshl_add_u64 v[192:193], v[56:57], 0, s[2:3]
	s_mov_b32 s6, 0x79000
	s_cmp_gt_i32 s4, 14
	s_cselect_b32 s2, s6, 0xb5000
	s_mov_b32 s3, 0
	v_lshl_add_u64 v[194:195], v[56:57], 0, s[2:3]
	v_mov_b32_e32 v199, 0xfffff
	s_mov_b32 s2, 0xfffeffff
.LBB0_97:
	global_load_dwordx4 v[104:107], v[192:193], off sc1
	global_load_dwordx4 v[100:103], v[192:193], off offset:1024 sc1
	global_load_dwordx4 v[96:99], v[192:193], off offset:2048 sc1
	global_load_dwordx4 v[88:91], v[192:193], off offset:3072 sc1
	global_load_dwordx4 v[80:83], v[194:195], off sc1
	global_load_dwordx4 v[72:75], v[194:195], off offset:1024 sc1
	global_load_dwordx4 v[64:67], v[194:195], off offset:2048 sc1
	global_load_dwordx4 v[56:59], v[194:195], off offset:3072 sc1
	s_waitcnt vmcnt(0)
	s_nop 0
	v_max_u32_e32 v200, v101, v103
	v_max_u32_e32 v201, v97, v99
	v_max_u32_e32 v202, v89, v91
	v_max3_u32 v200, v105, v107, v200
	v_max_u32_e32 v203, v81, v83
	v_max3_u32 v200, v200, v201, v202
	v_max_u32_e32 v201, v73, v75
	v_max3_u32 v200, v200, v203, v201
	v_max_u32_e32 v201, v65, v67
	v_max_u32_e32 v202, v57, v59
	v_max3_u32 v200, v200, v201, v202
	v_cmp_lt_u32_e32 vcc, s2, v200
	s_cmp_eq_u64 vcc, 0
	s_cselect_b64 s[6:7], -1, 0
	v_subrev_co_u32_e32 v199, vcc, 1, v199
	s_or_b64 s[6:7], s[6:7], vcc
	s_andn2_b64 vcc, exec, s[6:7]
	s_cbranch_vccnz .LBB0_97
	v_mfma_f32_16x16x32_f16 a[0:3], v[104:107], v[124:127], a[0:3]
	v_mfma_f32_16x16x32_f16 a[0:3], v[100:103], v[116:119], a[0:3]
	v_mfma_f32_16x16x32_f16 a[0:3], v[96:99], v[108:111], a[0:3]
	v_mfma_f32_16x16x32_f16 a[0:3], v[88:91], v[36:39], a[0:3]
	v_mfma_f32_16x16x32_f16 a[0:3], v[80:83], v[28:31], a[0:3]
	v_mfma_f32_16x16x32_f16 a[0:3], v[72:75], v[20:23], a[0:3]
	v_mfma_f32_16x16x32_f16 a[0:3], v[64:67], v[12:15], a[0:3]
	v_mfma_f32_16x16x32_f16 a[0:3], v[56:59], v[4:7], a[0:3]
	s_and_b64 exec, exec, s[0:1]
	s_cbranch_execz .LBB0_100
	s_mul_i32 s0, s4, 30
	v_mul_u32_u24_e32 v6, 0xe10, v196
	v_add3_u32 v6, s0, v197, v6
	s_nop 2
	v_accvgpr_read_b32 v0, a0
	s_waitcnt lgkmcnt(0)
	v_mov_b32_e32 v4, s12
	v_mov_b32_e32 v5, s13
	v_ashrrev_i32_e32 v7, 31, v6
	v_accvgpr_read_b32 v1, a1
	v_fmamk_f32 v0, v0, 0x3b800000, v198
	v_lshl_add_u64 v[4:5], v[6:7], 2, v[4:5]
	global_store_dword v[4:5], v0, off
	v_fmamk_f32 v0, v1, 0x3b800000, v198
	v_accvgpr_read_b32 v2, a2
	global_store_dword v[4:5], v0, off offset:3600
	v_add_co_u32_e32 v0, vcc, 0x1000, v4
	v_fmamk_f32 v2, v2, 0x3b800000, v198
	s_nop 0
	v_addc_co_u32_e32 v1, vcc, 0, v5, vcc
	v_accvgpr_read_b32 v3, a3
	global_store_dword v[0:1], v2, off offset:3104
	v_add_co_u32_e32 v0, vcc, 0x2000, v4
	v_fmac_f32_e32 v198, 0x3b800000, v3
	s_nop 0
	v_addc_co_u32_e32 v1, vcc, 0, v5, vcc
	global_store_dword v[0:1], v198, off offset:2608
